# P10 epilogue: bias of the next unit fetched late in the previous epilogue into v[224:239]; no bias loads and no vmcnt(0) drain at epilogue start
# baseline (speedup 1.0000x reference)
;     __device__ __forceinline__ void operator()(const f32x4 (&acc)[2][2][4][2], const Unit& u, int wr, int wc, int fr, int fq) const {
;         const int e = u.pn / npn, pnl = u.pn - e * npn; const int tid = threadIdx.x;
;         const int col0 = pnl * BM + wc * 32 + 8 * fq;
;         f32x4 bv[2][2];
; #pragma unroll
;         for (int bj = 0; bj < 2; ++bj)
; #pragma unroll
;             for (int n = 0; n < 2; ++n) bv[bj][n] = *(const f32x4*)(bias + (size_t)e * bias_ld + col0 + bj * HALF + 4 * n);
.LBB0_1141:
	s_min_i32 s42, s64, 64
	s_add_u32 s4, s96, 0xb3400000
	s_addc_u32 s5, s97, 0
	s_add_i32 s43, s34, 0x18000
	s_mov_b64 s[6:7], 0x80
	s_add_i32 s44, s34, 0x1a000
	v_lshl_add_u64 v[2:3], v[2:3], 0, s[6:7]
	s_mov_b32 m0, s43
	s_add_u32 s8, s24, 0x40080
	s_waitcnt vmcnt(2)
	s_barrier
	global_load_lds_dwordx4 v[2:3], off
	v_lshl_add_u64 v[2:3], v[4:5], 0, s[6:7]
	s_mov_b32 m0, s44
	s_addc_u32 s9, s25, 0
	s_add_i32 s45, s34, 0x1c000
	global_load_lds_dwordx4 v[2:3], off
	v_lshl_add_u64 v[2:3], s[8:9], 0, v[166:167]
	s_mov_b32 m0, s45
	s_add_i32 s46, s34, 0x1e000
	global_load_lds_dwordx4 v[2:3], off
	v_lshl_add_u64 v[2:3], s[8:9], 0, v[162:163]
	s_mov_b32 m0, s46
	v_lshlrev_b32_e32 v4, 4, v10
	global_load_lds_dwordx4 v[2:3], off
	v_and_b32_e32 v4, 0x38000, v4
	v_lshlrev_b32_e32 v5, 11, v12
	s_cmpk_lt_u32 s10, 0x100
	v_or3_b32 v4, v8, v4, v5
	s_mov_b32 s21, s2
	s_cselect_b64 s[10:11], -1, 0
	v_lshl_or_b32 v2, s12, 4, v7
	s_movk_i32 s2, 0x110
	v_bfe_u32 v3, v0, 4, 4
	s_add_i32 s3, 0, 0x21000
	v_add_u32_e32 v172, v4, v9
	v_lshlrev_b32_e32 v4, 8, v0
	s_waitcnt vmcnt(4)
	v_or_b32_e32 v186, s14, v6
	v_mul_lo_u32 v2, v2, s2
	v_and_or_b32 v187, v14, 64, v3
	s_add_i32 s14, s14, s3
	v_mov_b32_e32 v3, s3
	v_and_b32_e32 v4, 0x18000, v4
	v_and_b32_e32 v170, 0xf0, v11
	v_add_u32_e32 v2, s14, v2
	v_mad_u32_u24 v3, v13, s2, v3
	s_max_i32 s48, s42, 1
	v_or3_b32 v4, v8, v4, v5
	v_mov_b32_e32 v169, v167
	v_mov_b32_e32 v165, v167
	s_mov_b32 s49, 0
	s_mov_b32 s47, 0x18000
	s_mov_b64 s[8:9], 0x40080
	v_mov_b32_e32 v171, v167
	s_add_i32 s48, s48, -1
	v_mov_b32_e32 v173, v167
	v_add_u32_e32 v174, v4, v9
	v_mov_b32_e32 v175, v167
	s_mov_b32 s50, 0x8000
	s_mov_b32 s51, 0x10000
	s_mov_b32 s12, 0x3c800000
	v_add_u32_e32 v188, v2, v6
	v_add_u32_e32 v189, v3, v170
	s_mov_b32 s52, 0x40000
	s_mov_b32 s53, 0x48000
	s_ashr_i32 s98, s21, 31
	s_lshr_b32 s98, s98, 29
	s_add_i32 s98, s21, s98
	s_ashr_i32 s98, s98, 3
	s_lshl_b32 s99, s98, 11
	s_lshl_b32 s100, s21, 8
	s_sub_i32 s100, s100, s99
	v_or_b32_e32 v240, s100, v186
	v_ashrrev_i32_e32 v241, 31, v240
	s_ashr_i32 s99, s98, 31
	s_lshl_b64 s[98:99], s[98:99], 13
	v_readlane_b32 s100, v254, 4
	v_readlane_b32 s101, v254, 5
	s_nop 3
	s_add_u32 s98, s100, s98
	s_addc_u32 s99, s101, s99
	v_lshl_add_u64 v[240:241], v[240:241], 2, s[98:99]
	global_load_dwordx4 v[236:239], v[240:241], off
	global_load_dwordx4 v[232:235], v[240:241], off offset:16
	global_load_dwordx4 v[228:231], v[240:241], off offset:512
	global_load_dwordx4 v[224:227], v[240:241], off offset:528
	s_waitcnt vmcnt(0)
	s_barrier
	s_branch .LBB0_1144

; #define LAS __attribute__((address_space(3)))
; __device__ __forceinline__ unsigned pk4_fp8(float a, float b, float c, float d) { int w = 0; w = __builtin_amdgcn_cvt_pk_fp8_f32(a, b, w, false); w = __builtin_amdgcn_cvt_pk_fp8_f32(c, d, w, true); return (unsigned)w; }
;     __device__ __forceinline__ void operator()(const f32x4 (&acc)[2][2][4][2], const Unit& u, int wr, int wc, int fr, int fq) const {
;     ...
;                     for (int bj = 0; bj < 2; ++bj) { const int m = 2 * mp + ms; const f32x4 v0 = acc[ai][bj][m][0] * scale + bv[bj][0], v1 = acc[ai][bj][m][1] * scale + bv[bj][1];
;                         u32x2 w; w.x = pk4_fp8(v0[0], v0[1], v0[2], v0[3]); w.y = pk4_fp8(v1[0], v1[1], v1[2], v1[3]);
;                         *(LAS u32x2*)(wp + ms * SLAB + 128 * bj) = w; }
;                 asm volatile("s_waitcnt lgkmcnt(0)" ::: "memory"); __builtin_amdgcn_s_barrier(); asm volatile("" ::: "memory");
; #pragma unroll
;                 for (int ms = 0; ms < 2; ++ms) *(u32x4*)(gp + (size_t)(ai * HALF + (2 * mp + ms) * 16) * ldc) = *(const LAS u32x4*)(rp + ms * SLAB);
;                 asm volatile("s_waitcnt lgkmcnt(0)" ::: "memory"); __builtin_amdgcn_s_barrier(); asm volatile("" ::: "memory");
.LBB0_1150:
	s_ashr_i32 s2, s21, 31
	s_lshr_b32 s2, s2, 29
	s_add_i32 s2, s21, s2
	s_ashr_i32 s2, s2, 3
	s_lshl_b32 s3, s2, 11
	s_lshl_b32 s21, s21, 8
	v_readlane_b32 s56, v254, 0
	s_sub_i32 s22, s21, s3
	s_ashr_i32 s3, s2, 31
	v_readlane_b32 s60, v254, 4
	v_readlane_b32 s61, v254, 5
	s_lshl_b64 s[2:3], s[2:3], 13
	v_readlane_b32 s62, v254, 6
	v_readlane_b32 s63, v254, 7
	s_mov_b64 s[24:25], s[60:61]
	v_or_b32_e32 v2, s22, v186
	s_add_u32 s2, s24, s2
	s_addc_u32 s3, s25, s3
	v_ashrrev_i32_e32 v3, 31, v2
	s_nop 15
	s_nop 15
	v_lshl_add_u64 v[2:3], v[2:3], 2, s[2:3]
	s_nop 0
	v_mov_b32_e32 v20, 0
	v_mov_b32_e32 v21, 0
	v_mov_b32_e32 v22, 0
	v_mov_b32_e32 v23, 0
	v_mov_b32_e32 v24, 0
	v_mov_b32_e32 v25, 0
	v_mov_b32_e32 v26, 0
	v_mov_b32_e32 v27, 0
	v_lshl_or_b32 v18, s20, 8, v187
	v_add_u32_e32 v178, 0x2000, v188
	v_ashrrev_i32_e32 v19, 31, v18
	v_lshlrev_b64 v[18:19], 11, v[18:19]
	v_mov_b32_e32 v32, 0
	v_mov_b32_e32 v33, 0
	v_lshl_add_u64 v[18:19], s[4:5], 0, v[18:19]
	s_ashr_i32 s23, s22, 31
	v_lshl_add_u64 v[18:19], v[18:19], 0, s[22:23]
	v_lshl_add_u64 v[18:19], v[18:19], 0, v[170:171]
	v_add_co_u32_e32 v176, vcc, s50, v18
	v_mov_b32_e32 v28, 0
	v_mov_b32_e32 v29, 0
	v_mov_b32_e32 v30, 0
	v_mov_b32_e32 v31, 0
	v_addc_co_u32_e32 v177, vcc, 0, v19, vcc
	s_cmp_eq_u32 s49, s48
	s_mov_b64 s[2:3], -1
	v_readlane_b32 s57, v254, 1
	v_readlane_b32 s58, v254, 2
	v_readlane_b32 s59, v254, 3
	s_mov_b64 s[26:27], s[62:63]
	v_pk_fma_f32 v[158:159], v[158:159], s[12:13], v[236:237] op_sel_hi:[1,0,1]
	v_pk_fma_f32 v[154:155], v[154:155], s[12:13], v[232:233] op_sel_hi:[1,0,1]
	v_pk_fma_f32 v[138:139], v[138:139], s[12:13], v[228:229] op_sel_hi:[1,0,1]
	v_pk_fma_f32 v[130:131], v[130:131], s[12:13], v[224:225] op_sel_hi:[1,0,1]
	v_pk_fma_f32 v[150:151], v[150:151], s[12:13], v[236:237] op_sel_hi:[1,0,1]
	v_pk_fma_f32 v[146:147], v[146:147], s[12:13], v[232:233] op_sel_hi:[1,0,1]
	v_pk_fma_f32 v[126:127], v[126:127], s[12:13], v[228:229] op_sel_hi:[1,0,1]
	v_pk_fma_f32 v[122:123], v[122:123], s[12:13], v[224:225] op_sel_hi:[1,0,1]
	v_cvt_pk_fp8_f32 v20, v158, v159
	v_cvt_pk_fp8_f32 v21, v154, v155
	v_cvt_pk_fp8_f32 v22, v138, v139
	v_cvt_pk_fp8_f32 v23, v130, v131
	v_cvt_pk_fp8_f32 v24, v150, v151
	v_cvt_pk_fp8_f32 v25, v146, v147
	v_cvt_pk_fp8_f32 v26, v126, v127
	v_cvt_pk_fp8_f32 v27, v122, v123
	v_pk_fma_f32 v[160:161], v[160:161], s[12:13], v[238:239] op_sel_hi:[1,0,1]
	v_pk_fma_f32 v[156:157], v[156:157], s[12:13], v[234:235] op_sel_hi:[1,0,1]
	v_pk_fma_f32 v[140:141], v[140:141], s[12:13], v[230:231] op_sel_hi:[1,0,1]
	v_pk_fma_f32 v[132:133], v[132:133], s[12:13], v[226:227] op_sel_hi:[1,0,1]
	v_pk_fma_f32 v[152:153], v[152:153], s[12:13], v[238:239] op_sel_hi:[1,0,1]
	v_pk_fma_f32 v[148:149], v[148:149], s[12:13], v[234:235] op_sel_hi:[1,0,1]
	v_pk_fma_f32 v[128:129], v[128:129], s[12:13], v[230:231] op_sel_hi:[1,0,1]
	v_pk_fma_f32 v[124:125], v[124:125], s[12:13], v[226:227] op_sel_hi:[1,0,1]
	v_cvt_pk_fp8_f32 v20, v160, v161 op_sel:[0,0,1]
	v_cvt_pk_fp8_f32 v21, v156, v157 op_sel:[0,0,1]
	v_cvt_pk_fp8_f32 v22, v140, v141 op_sel:[0,0,1]
	v_cvt_pk_fp8_f32 v23, v132, v133 op_sel:[0,0,1]
	v_cvt_pk_fp8_f32 v24, v152, v153 op_sel:[0,0,1]
	v_cvt_pk_fp8_f32 v25, v148, v149 op_sel:[0,0,1]
	v_cvt_pk_fp8_f32 v26, v128, v129 op_sel:[0,0,1]
	v_cvt_pk_fp8_f32 v27, v124, v125 op_sel:[0,0,1]
	ds_write2_b64 v188, v[20:21], v[22:23] offset1:16
	ds_write2_b64 v178, v[24:25], v[26:27] offset0:64 offset1:80
	s_waitcnt lgkmcnt(0)
	s_barrier
	ds_read_b128 v[20:23], v189
	ds_read_b128 v[24:27], v189 offset:8704
	v_pk_fma_f32 v[110:111], v[110:111], s[12:13], v[236:237] op_sel_hi:[1,0,1]
	v_pk_fma_f32 v[106:107], v[106:107], s[12:13], v[232:233] op_sel_hi:[1,0,1]
	v_cvt_pk_fp8_f32 v32, v110, v111
	v_cvt_pk_fp8_f32 v33, v106, v107
	v_pk_fma_f32 v[142:143], v[142:143], s[12:13], v[236:237] op_sel_hi:[1,0,1]
	v_pk_fma_f32 v[134:135], v[134:135], s[12:13], v[232:233] op_sel_hi:[1,0,1]
	v_pk_fma_f32 v[118:119], v[118:119], s[12:13], v[228:229] op_sel_hi:[1,0,1]
	v_pk_fma_f32 v[114:115], v[114:115], s[12:13], v[224:225] op_sel_hi:[1,0,1]
	s_waitcnt lgkmcnt(1)
	global_store_dwordx4 v[18:19], v[20:23], off
	s_waitcnt lgkmcnt(0)
	global_store_dwordx4 v[176:177], v[24:27], off
	v_cvt_pk_fp8_f32 v28, v142, v143
	v_pk_fma_f32 v[20:21], v[112:113], s[12:13], v[238:239] op_sel_hi:[1,0,1]
	v_pk_fma_f32 v[22:23], v[108:109], s[12:13], v[234:235] op_sel_hi:[1,0,1]
	v_cvt_pk_fp8_f32 v29, v134, v135
	v_cvt_pk_fp8_f32 v30, v118, v119
	v_cvt_pk_fp8_f32 v31, v114, v115
	v_cvt_pk_fp8_f32 v32, v20, v21 op_sel:[0,0,1]
	v_cvt_pk_fp8_f32 v33, v22, v23 op_sel:[0,0,1]
	v_pk_fma_f32 v[20:21], v[102:103], s[12:13], v[228:229] op_sel_hi:[1,0,1]
	v_pk_fma_f32 v[22:23], v[98:99], s[12:13], v[224:225] op_sel_hi:[1,0,1]
	v_mov_b32_e32 v24, 0
	v_mov_b32_e32 v25, 0
	v_cvt_pk_fp8_f32 v24, v20, v21
	v_cvt_pk_fp8_f32 v25, v22, v23
	v_pk_fma_f32 v[144:145], v[144:145], s[12:13], v[238:239] op_sel_hi:[1,0,1]
	v_pk_fma_f32 v[136:137], v[136:137], s[12:13], v[234:235] op_sel_hi:[1,0,1]
	v_pk_fma_f32 v[120:121], v[120:121], s[12:13], v[230:231] op_sel_hi:[1,0,1]
	v_pk_fma_f32 v[116:117], v[116:117], s[12:13], v[226:227] op_sel_hi:[1,0,1]
	v_cvt_pk_fp8_f32 v28, v144, v145 op_sel:[0,0,1]
	v_cvt_pk_fp8_f32 v29, v136, v137 op_sel:[0,0,1]
	v_cvt_pk_fp8_f32 v30, v120, v121 op_sel:[0,0,1]
	v_cvt_pk_fp8_f32 v31, v116, v117 op_sel:[0,0,1]
	v_pk_fma_f32 v[20:21], v[104:105], s[12:13], v[230:231] op_sel_hi:[1,0,1]
	v_pk_fma_f32 v[22:23], v[100:101], s[12:13], v[226:227] op_sel_hi:[1,0,1]
	v_cvt_pk_fp8_f32 v24, v20, v21 op_sel:[0,0,1]
	v_cvt_pk_fp8_f32 v25, v22, v23 op_sel:[0,0,1]
	s_waitcnt lgkmcnt(0)
	s_barrier
; #define LAS __attribute__((address_space(3)))
; __device__ __forceinline__ unsigned pk4_fp8(float a, float b, float c, float d) { int w = 0; w = __builtin_amdgcn_cvt_pk_fp8_f32(a, b, w, false); w = __builtin_amdgcn_cvt_pk_fp8_f32(c, d, w, true); return (unsigned)w; }
;     __device__ __forceinline__ void operator()(const f32x4 (&acc)[2][2][4][2], const Unit& u, int wr, int wc, int fr, int fq) const {
;     ...
;                     for (int bj = 0; bj < 2; ++bj) { const int m = 2 * mp + ms; const f32x4 v0 = acc[ai][bj][m][0] * scale + bv[bj][0], v1 = acc[ai][bj][m][1] * scale + bv[bj][1];
;                         u32x2 w; w.x = pk4_fp8(v0[0], v0[1], v0[2], v0[3]); w.y = pk4_fp8(v1[0], v1[1], v1[2], v1[3]);
;                         *(LAS u32x2*)(wp + ms * SLAB + 128 * bj) = w; }
;                 asm volatile("s_waitcnt lgkmcnt(0)" ::: "memory"); __builtin_amdgcn_s_barrier(); asm volatile("" ::: "memory");
; #pragma unroll
;                 for (int ms = 0; ms < 2; ++ms) *(u32x4*)(gp + (size_t)(ai * HALF + (2 * mp + ms) * 16) * ldc) = *(const LAS u32x4*)(rp + ms * SLAB);
;                 asm volatile("s_waitcnt lgkmcnt(0)" ::: "memory"); __builtin_amdgcn_s_barrier(); asm volatile("" ::: "memory");
	ds_write2_b64 v188, v[28:29], v[30:31] offset1:16
	ds_write2_b64 v178, v[32:33], v[24:25] offset0:64 offset1:80
	s_waitcnt lgkmcnt(0)
	s_barrier
	ds_read_b128 v[20:23], v189
	ds_read_b128 v[24:27], v189 offset:8704
	v_add_co_u32_e32 v28, vcc, s51, v18
	v_mov_b32_e32 v30, 0
	s_nop 0
	v_addc_co_u32_e32 v29, vcc, 0, v19, vcc
	s_waitcnt lgkmcnt(1)
	global_store_dwordx4 v[28:29], v[20:23], off
	v_mov_b32_e32 v28, 0
	v_mov_b32_e32 v29, 0
	v_add_co_u32_e32 v20, vcc, s47, v18
	v_pk_fma_f32 v[22:23], v[90:91], s[12:13], v[232:233] op_sel_hi:[1,0,1]
	s_nop 0
	v_addc_co_u32_e32 v21, vcc, 0, v19, vcc
	s_waitcnt lgkmcnt(0)
	global_store_dwordx4 v[20:21], v[24:27], off
	v_pk_fma_f32 v[20:21], v[94:95], s[12:13], v[236:237] op_sel_hi:[1,0,1]
	v_mov_b32_e32 v31, 0
	v_mov_b32_e32 v24, 0
	v_mov_b32_e32 v25, 0
	v_cvt_pk_fp8_f32 v24, v20, v21
	v_cvt_pk_fp8_f32 v25, v22, v23
	v_pk_fma_f32 v[20:21], v[96:97], s[12:13], v[238:239] op_sel_hi:[1,0,1]
	v_pk_fma_f32 v[22:23], v[92:93], s[12:13], v[234:235] op_sel_hi:[1,0,1]
	v_cvt_pk_fp8_f32 v24, v20, v21 op_sel:[0,0,1]
	v_cvt_pk_fp8_f32 v25, v22, v23 op_sel:[0,0,1]
	v_pk_fma_f32 v[20:21], v[82:83], s[12:13], v[228:229] op_sel_hi:[1,0,1]
	v_pk_fma_f32 v[22:23], v[74:75], s[12:13], v[224:225] op_sel_hi:[1,0,1]
	v_mov_b32_e32 v26, 0
	v_mov_b32_e32 v27, 0
	v_cvt_pk_fp8_f32 v26, v20, v21
	v_cvt_pk_fp8_f32 v27, v22, v23
	v_pk_fma_f32 v[20:21], v[84:85], s[12:13], v[230:231] op_sel_hi:[1,0,1]
	v_pk_fma_f32 v[22:23], v[76:77], s[12:13], v[226:227] op_sel_hi:[1,0,1]
	v_cvt_pk_fp8_f32 v26, v20, v21 op_sel:[0,0,1]
	v_cvt_pk_fp8_f32 v27, v22, v23 op_sel:[0,0,1]
	v_pk_fma_f32 v[20:21], v[86:87], s[12:13], v[236:237] op_sel_hi:[1,0,1]
	v_pk_fma_f32 v[22:23], v[78:79], s[12:13], v[232:233] op_sel_hi:[1,0,1]
	v_cvt_pk_fp8_f32 v28, v20, v21
	v_cvt_pk_fp8_f32 v29, v22, v23
	v_pk_fma_f32 v[20:21], v[88:89], s[12:13], v[238:239] op_sel_hi:[1,0,1]
	v_pk_fma_f32 v[22:23], v[80:81], s[12:13], v[234:235] op_sel_hi:[1,0,1]
	v_cvt_pk_fp8_f32 v28, v20, v21 op_sel:[0,0,1]
	v_cvt_pk_fp8_f32 v29, v22, v23 op_sel:[0,0,1]
	v_pk_fma_f32 v[20:21], v[70:71], s[12:13], v[228:229] op_sel_hi:[1,0,1]
	v_pk_fma_f32 v[22:23], v[66:67], s[12:13], v[224:225] op_sel_hi:[1,0,1]
	v_cvt_pk_fp8_f32 v30, v20, v21
	v_cvt_pk_fp8_f32 v31, v22, v23
	v_pk_fma_f32 v[20:21], v[72:73], s[12:13], v[230:231] op_sel_hi:[1,0,1]
	v_pk_fma_f32 v[22:23], v[68:69], s[12:13], v[226:227] op_sel_hi:[1,0,1]
	v_cvt_pk_fp8_f32 v30, v20, v21 op_sel:[0,0,1]
	v_cvt_pk_fp8_f32 v31, v22, v23 op_sel:[0,0,1]
	s_waitcnt lgkmcnt(0)
	s_barrier
	ds_write2_b64 v188, v[24:25], v[26:27] offset1:16
	ds_write2_b64 v178, v[28:29], v[30:31] offset0:64 offset1:80
	s_waitcnt lgkmcnt(0)
	s_barrier
	ds_read_b128 v[20:23], v189
	ds_read_b128 v[24:27], v189 offset:8704
	v_add_co_u32_e32 v28, vcc, s52, v18
	s_nop 1
	v_addc_co_u32_e32 v29, vcc, 0, v19, vcc
	s_waitcnt lgkmcnt(1)
	global_store_dwordx4 v[28:29], v[20:23], off
	s_nop 1
	v_add_co_u32_e32 v20, vcc, s53, v18
	v_pk_fma_f32 v[22:23], v[58:59], s[12:13], v[232:233] op_sel_hi:[1,0,1]
	s_nop 0
	v_addc_co_u32_e32 v21, vcc, 0, v19, vcc
	s_waitcnt lgkmcnt(0)
	global_store_dwordx4 v[20:21], v[24:27], off
	v_pk_fma_f32 v[20:21], v[62:63], s[12:13], v[236:237] op_sel_hi:[1,0,1]
	v_pk_fma_f32 v[14:15], v[54:55], s[12:13], v[236:237] op_sel_hi:[1,0,1]
	v_mov_b32_e32 v24, 0
	v_cvt_pk_fp8_f32 v24, v20, v21
	v_pk_fma_f32 v[20:21], v[64:65], s[12:13], v[238:239] op_sel_hi:[1,0,1]
	v_mov_b32_e32 v26, 0
	v_mov_b32_e32 v25, 0
	v_cvt_pk_fp8_f32 v24, v20, v21 op_sel:[0,0,1]
	v_pk_fma_f32 v[20:21], v[50:51], s[12:13], v[228:229] op_sel_hi:[1,0,1]
	v_cvt_pk_fp8_f32 v25, v22, v23
	v_cvt_pk_fp8_f32 v26, v20, v21
	v_pk_fma_f32 v[20:21], v[52:53], s[12:13], v[230:231] op_sel_hi:[1,0,1]
	v_pk_fma_f32 v[22:23], v[60:61], s[12:13], v[234:235] op_sel_hi:[1,0,1]
	v_pk_fma_f32 v[10:11], v[46:47], s[12:13], v[232:233] op_sel_hi:[1,0,1]
	v_cvt_pk_fp8_f32 v26, v20, v21 op_sel:[0,0,1]
	v_mov_b32_e32 v20, 0
	v_cvt_pk_fp8_f32 v20, v14, v15
	v_mov_b32_e32 v21, 0
	v_cvt_pk_fp8_f32 v25, v22, v23 op_sel:[0,0,1]
	v_pk_fma_f32 v[22:23], v[42:43], s[12:13], v[224:225] op_sel_hi:[1,0,1]
	v_mov_b32_e32 v27, 0
	v_cvt_pk_fp8_f32 v21, v10, v11
	v_pk_fma_f32 v[10:11], v[56:57], s[12:13], v[238:239] op_sel_hi:[1,0,1]
	v_cvt_pk_fp8_f32 v27, v22, v23
	v_cvt_pk_fp8_f32 v20, v10, v11 op_sel:[0,0,1]
	v_pk_fma_f32 v[6:7], v[38:39], s[12:13], v[228:229] op_sel_hi:[1,0,1]
	v_pk_fma_f32 v[2:3], v[34:35], s[12:13], v[224:225] op_sel_hi:[1,0,1]
	v_mov_b32_e32 v10, 0
	v_mov_b32_e32 v11, 0
	v_cvt_pk_fp8_f32 v10, v6, v7
	v_cvt_pk_fp8_f32 v11, v2, v3
	v_pk_fma_f32 v[22:23], v[44:45], s[12:13], v[226:227] op_sel_hi:[1,0,1]
	v_pk_fma_f32 v[12:13], v[48:49], s[12:13], v[234:235] op_sel_hi:[1,0,1]
	v_cvt_pk_fp8_f32 v27, v22, v23 op_sel:[0,0,1]
	v_pk_fma_f32 v[2:3], v[40:41], s[12:13], v[230:231] op_sel_hi:[1,0,1]
	v_pk_fma_f32 v[4:5], v[36:37], s[12:13], v[226:227] op_sel_hi:[1,0,1]
	s_cbranch_scc1 .Lp10_nb_skip
	s_ashr_i32 s98, s15, 31
	s_lshr_b32 s98, s98, 29
	s_add_i32 s98, s15, s98
	s_ashr_i32 s98, s98, 3
	s_lshl_b32 s99, s98, 11
	s_lshl_b32 s100, s15, 8
	s_sub_i32 s100, s100, s99
	v_or_b32_e32 v240, s100, v186
	v_ashrrev_i32_e32 v241, 31, v240
	s_ashr_i32 s99, s98, 31
	s_lshl_b64 s[98:99], s[98:99], 13
	v_readlane_b32 s100, v254, 4
	v_readlane_b32 s101, v254, 5
	s_nop 3
	s_add_u32 s98, s100, s98
	s_addc_u32 s99, s101, s99
	v_lshl_add_u64 v[240:241], v[240:241], 2, s[98:99]
	global_load_dwordx4 v[236:239], v[240:241], off
	global_load_dwordx4 v[232:235], v[240:241], off offset:16
	global_load_dwordx4 v[228:231], v[240:241], off offset:512
	global_load_dwordx4 v[224:227], v[240:241], off offset:528
.Lp10_nb_skip:
	s_cmp_eq_u32 s49, s48
	v_cvt_pk_fp8_f32 v21, v12, v13 op_sel:[0,0,1]
	v_cvt_pk_fp8_f32 v10, v2, v3 op_sel:[0,0,1]
	v_cvt_pk_fp8_f32 v11, v4, v5 op_sel:[0,0,1]
	s_waitcnt lgkmcnt(0)
	s_barrier
	ds_write2_b64 v188, v[24:25], v[26:27] offset1:16
	ds_write2_b64 v178, v[20:21], v[10:11] offset0:64 offset1:80
	s_waitcnt lgkmcnt(0)
	s_barrier
	ds_read_b128 v[2:5], v189
	ds_read_b128 v[6:9], v189 offset:8704
	v_add_co_u32_e32 v10, vcc, 0x50000, v18
	s_nop 1
	v_addc_co_u32_e32 v11, vcc, 0, v19, vcc
	s_waitcnt lgkmcnt(1)
	global_store_dwordx4 v[10:11], v[2:5], off
	s_nop 1
	v_add_co_u32_e32 v2, vcc, 0x58000, v18
	s_nop 1
	v_addc_co_u32_e32 v3, vcc, 0, v19, vcc
	s_waitcnt lgkmcnt(0)
	global_store_dwordx4 v[2:3], v[6:9], off
	s_waitcnt lgkmcnt(0)
	s_barrier
	s_cbranch_scc1 .LBB0_1143
	s_andn2_b64 vcc, exec, s[0:1]
	s_cbranch_vccnz .LBB0_1142
	s_barrier
	s_branch .LBB0_1142
